# attention phase: half of the workgroups (bit 3 of the index) run the memory-bound short-conv part before the attention part, so it overlaps the other half's attention
# baseline (speedup 1.0000x reference)
_Z3fwdILj131071EEv4Args:
	v_mov_b32_e32 v255, 0
	s_load_dwordx2 s[8:9], s[0:1], 0x130
	s_load_dwordx4 s[4:7], s[0:1], 0x138
	v_writelane_b32 v243, s2, 0
	s_nop 1
	v_writelane_b32 v243, s3, 1
	s_waitcnt lgkmcnt(0)
	v_writelane_b32 v243, s4, 2
	v_readfirstlane_b32 s2, v0
	s_and_b32 s33, s2, 0xffffffc0
	v_writelane_b32 v243, s5, 3
	v_mbcnt_lo_u32_b32 v0, -1, 0
	v_mbcnt_hi_u32_b32 v0, -1, v0
	v_writelane_b32 v243, s6, 4
	v_add_u32_e32 v0, s33, v0
	v_writelane_b32 v243, s7, 5
	v_cmp_gt_i32_e32 vcc, 16, v0
	v_writelane_b32 v243, s2, 6
	s_and_saveexec_b64 s[2:3], vcc
	v_lshl_add_u32 v1, v0, 2, 0
	v_add_u32_e32 v1, 0x27fc0, v1
	v_mov_b32_e32 v2, 0
	ds_write_b32 v1, v2
	s_or_b64 exec, exec, s[2:3]
	v_writelane_b32 v243, s0, 7
	s_load_dwordx4 s[4:7], s[0:1], 0x138
	s_waitcnt lgkmcnt(0)
	v_writelane_b32 v243, s1, 8
	s_barrier
	s_mul_i32 s2, s6, 0xd80
	s_ashr_i32 s3, s2, 31
	s_lshl_b64 s[2:3], s[2:3], 2
	s_add_u32 s0, s8, s2
	s_addc_u32 s1, s9, s3
	s_add_u32 s60, s0, 0x4000
	s_addc_u32 s61, s1, 0
	s_sub_i32 s0, s5, s4
	s_cmp_lt_i32 s0, 2
	s_mov_b32 s0, 0
	v_writelane_b32 v243, s0, 9
	s_cbranch_scc1 .LBB0_7
	s_getreg_b32 s0, hwreg(HW_REG_XCC_ID, 0, 4)
	s_and_b32 s0, s0, 15
	v_cmp_eq_u32_e32 vcc, 0, v0
	v_writelane_b32 v243, s0, 9
	s_and_saveexec_b64 s[0:1], vcc
	s_cbranch_execz .LBB0_6
	s_mov_b64 s[2:3], exec
	v_mbcnt_lo_u32_b32 v0, s2, 0
	v_mbcnt_hi_u32_b32 v0, s3, v0
	v_cmp_eq_u32_e32 vcc, 0, v0
	s_and_b64 s[4:5], exec, vcc
	s_mov_b64 exec, s[4:5]
	s_cbranch_execz .LBB0_6
	v_readlane_b32 s4, v243, 9
	s_lshl_b32 s4, s4, 8
	s_bcnt1_i32_b64 s2, s[2:3]
	v_mov_b32_e32 v0, s4
	v_mov_b32_e32 v1, s2
	global_atomic_add v0, v1, s[60:61] offset:1024

.LBB0_360:
	v_readlane_b32 s12, v243, 7
	v_readlane_b32 s13, v243, 8
	s_load_dword s28, s[12:13], 0x148
	s_andn2_b64 vcc, exec, s[0:1]
	v_add_u32_e32 v86, s33, v0
	v_readlane_b32 s14, v255, 0
	s_nop 1
	s_cmp_lg_u32 s14, 0
	s_cbranch_scc1 .Lp3_A_done
	s_bitcmp1_b32 s2, 3
	s_cbranch_scc0 .Lp3_A_done
	s_mov_b32 s14, 1
	s_nop 1
	v_writelane_b32 v255, s14, 0
	v_mov_b32_e32 v78, v87
	s_branch .LBB0_390
.Lp3_A_done:
	s_cbranch_vccnz .LBB0_390
	v_readlane_b32 s1, v243, 6
	s_cmpk_lt_u32 s1, 0x800
	v_ashrrev_i32_e32 v89, 4, v0
	s_cselect_b64 s[14:15], -1, 0
	s_cmpk_gt_u32 s1, 0x7ff
	s_cselect_b64 s[16:17], -1, 0
	s_cmpk_lt_u32 s1, 0x1200
	v_lshlrev_b32_e32 v68, 3, v89
	v_bfe_u32 v4, v0, 2, 2
	s_cselect_b64 s[18:19], -1, 0
	v_or_b32_e32 v91, v4, v68
	v_and_b32_e32 v93, 8, v87
	s_add_i32 s38, 0, 0x1a000
	v_or_b32_e32 v2, s38, v93
	v_or_b32_e32 v3, 4, v91
	v_and_b32_e32 v5, 3, v0
	v_lshl_add_u32 v7, v91, 7, v2
	v_lshl_add_u32 v9, v3, 7, v2
	v_lshlrev_b32_e32 v2, 2, v89
	v_lshl_or_b32 v90, v4, 3, v5
	v_ashrrev_i32_e32 v3, 31, v2
	v_bitop3_b32 v6, v89, v4, 7 bitop3:0x6c
	v_lshl_add_u64 v[70:71], v[2:3], 1, s[8:9]
	v_lshlrev_b32_e32 v2, 7, v90
	v_bitop3_b32 v3, v4, v0, 3 bitop3:0x78
	v_add_u32_e32 v95, 4, v89
	v_bitop3_b32 v4, v5, v4, 4 bitop3:0x36
	v_bfe_u32 v92, v0, 1, 1
	v_or_b32_e32 v10, 0x12000, v2
	v_or_b32_e32 v2, 0x12200, v2
	v_xor_b32_e32 v5, v4, v89
	v_xor_b32_e32 v4, v4, v95
	v_bitop3_b32 v8, v91, v89, 4 bitop3:0x36
	v_lshl_add_u32 v97, v5, 4, v2
	v_lshl_add_u32 v98, v4, 4, v2
	v_xor_b32_e32 v2, v6, v92
	v_lshl_add_u32 v99, v2, 4, v7
	v_bitop3_b32 v2, v8, v92, 7 bitop3:0x6c
	v_or_b32_e32 v101, 2, v92
	v_lshl_add_u32 v100, v2, 4, v9
	v_xor_b32_e32 v2, v6, v101
	v_lshl_add_u32 v102, v2, 4, v7
	v_bitop3_b32 v2, v8, v101, 7 bitop3:0x6c
	v_or_b32_e32 v104, 4, v92
	v_lshl_add_u32 v103, v2, 4, v9
	v_xor_b32_e32 v2, v6, v104
	v_lshl_add_u32 v105, v2, 4, v7
	v_bitop3_b32 v2, v8, v104, 7 bitop3:0x6c
	v_or_b32_e32 v107, 6, v92
	s_load_dwordx2 s[12:13], s[10:11], 0x60
	v_xor_b32_e32 v11, v3, v89
	v_xor_b32_e32 v3, v3, v95
	v_lshl_add_u32 v106, v2, 4, v9
	v_xor_b32_e32 v2, v6, v107
	v_lshl_add_u32 v96, v3, 4, v10
	v_lshl_add_u32 v108, v2, 4, v7
	v_bitop3_b32 v2, v8, v107, 7 bitop3:0x6c
	s_lshl_b32 s0, s94, 4
	v_lshl_add_u32 v94, v11, 4, v10
	v_xor_b32_e32 v3, 64, v96
	v_lshl_add_u32 v109, v2, 4, v9
	v_and_b32_e32 v2, 31, v0
	v_ashrrev_i32_e32 v6, 5, v86
	s_lshl_b32 s20, s94, 10
	v_ashrrev_i32_e32 v1, 3, v0
	v_ashrrev_i32_e32 v69, 31, v68
	s_add_i32 s29, s0, 0x8000
	s_and_b32 s31, s0, 48
	v_xor_b32_e32 v11, 64, v94
	v_xor_b32_e32 v5, 64, v97
	v_xor_b32_e32 v4, 64, v98
	s_movk_i32 s0, 0x1e0
	s_mov_b32 s24, s2
	v_mad_u64_u32 v[72:73], s[22:23], v6, 31, v[2:3]
	s_add_i32 s34, 0, 0x22000
	s_add_i32 s36, s20, 0
	v_mbcnt_lo_u32_b32 v123, -1, 0
	v_and_b32_e32 v88, 15, v0
	s_lshr_b32 s30, s1, 8
	s_mov_b32 s21, 0
	v_xor_b32_e32 v110, 64, v99
	v_xor_b32_e32 v111, 64, v100
	v_xor_b32_e32 v112, 64, v102
	v_xor_b32_e32 v113, 64, v103
	v_xor_b32_e32 v114, 64, v105
	v_xor_b32_e32 v115, 64, v106
	v_xor_b32_e32 v116, 64, v108
	v_xor_b32_e32 v117, 64, v109
	v_cmp_gt_i32_e64 s[0:1], s0, v86
	v_cmp_ne_u32_e64 s[2:3], 31, v2
	v_lshl_add_u32 v73, v86, 2, s34
	v_xor_b32_e32 v118, v1, v0
	v_lshl_add_u64 v[74:75], v[68:69], 1, s[6:7]
	s_add_i32 s35, s94, -8
	s_add_i32 s37, s36, 0x12000
	v_lshl_add_u32 v69, s94, 3, v1
	s_add_i32 s38, s38, s20
	s_movk_i32 s39, 0x1400
	v_mov_b32_e32 v77, 0
	s_mov_b32 s40, 0xf149f2ca
	v_add_u32_e32 v119, 0, v11
	v_add_u32_e32 v120, 0, v3
	v_add_u32_e32 v121, 0, v5
	v_add_u32_e32 v122, 0, v4
	v_mbcnt_hi_u32_b32 v124, -1, v123
	s_mov_b32 s41, s24
	s_branch .LBB0_363

.LBB0_390:
	v_readlane_b32 s0, v255, 0
	s_nop 1
	s_cmp_eq_u32 s0, 2
	s_cbranch_scc1 .LBB0_409
	s_lshl_b32 s0, s2, 3
	s_add_i32 s16, s94, s0
	s_cmpk_gt_i32 s16, 0x17ff
	s_cbranch_scc1 .LBB0_409
	s_load_dwordx4 s[0:3], s[10:11], 0x68
	v_ashrrev_i32_e32 v79, 31, v78
	v_lshlrev_b64 v[0:1], 2, v[78:79]
	s_mov_b64 s[10:11], 0x1000
	s_waitcnt lgkmcnt(0)
	s_lshl_b32 s17, s28, 3
	v_lshl_add_u64 v[16:17], s[0:1], 0, v[0:1]
	s_movk_i32 s0, 0x1000
	v_add_co_u32_e32 v36, vcc, s0, v16
	v_lshl_add_u64 v[32:33], v[16:17], 0, s[10:11]
	s_nop 0
	v_addc_co_u32_e32 v37, vcc, 0, v17, vcc
	v_lshl_add_u64 v[34:35], s[2:3], 0, v[0:1]
	global_load_dwordx4 v[0:3], v[16:17], off offset:16
	global_load_dwordx4 v[4:7], v[16:17], off
	global_load_dwordx4 v[8:11], v[16:17], off offset:2064
	global_load_dwordx4 v[12:15], v[16:17], off offset:2048
	s_nop 0
	global_load_dwordx4 v[16:19], v[36:37], off
	global_load_dwordx4 v[20:23], v[32:33], off offset:16
	global_load_dwordx4 v[24:27], v[34:35], off offset:16
	global_load_dwordx4 v[28:31], v[34:35], off
	v_readlane_b32 s0, v243, 0
	v_readlane_b32 s1, v243, 1
	s_mov_b32 s2, s0
	s_mul_i32 s0, s0, 0x3c000
	s_mul_i32 s1, s94, 0x7800
	v_lshlrev_b64 v[32:33], 1, v[78:79]
	s_add_i32 s18, s0, s1
	s_mul_i32 s0, s2, 48
	s_mul_i32 s1, s94, 6
	v_lshl_add_u64 v[80:81], s[6:7], 0, v[32:33]
	v_lshl_add_u64 v[82:83], s[8:9], 0, v[32:33]
	s_mul_i32 s19, s28, 0x3c000
	s_add_i32 s0, s0, s1
	s_mul_i32 s20, s28, 48
	s_movk_i32 s21, 0x800
	s_movk_i32 s22, 0x7fe
	s_movk_i32 s23, 0x7ff
	v_mov_b32_e32 v84, 0x1400
	s_branch .LBB0_393

.LBB0_409:
	v_readlane_b32 s6, v255, 0
	s_nop 1
	s_cmp_eq_u32 s6, 1
	s_cbranch_scc0 .Lp3_C_done
	s_mov_b32 s6, 2
	s_nop 1
	v_writelane_b32 v255, s6, 0
	s_branch .LBB0_355
